# stack of five individually sub-noise changes on v34: P2c oa_finish/memattn order swap on odd workgroups, DSA staging write at top of half-iteration, one indexer barrier per item less, batched Gram-epi
# speedup vs baseline: 1.0039x; 1.0039x over previous
.LBB0_564:
	s_cmpk_gt_u32 s33, 0x43f
	s_cbranch_scc1 .LBB0_1240
	s_add_u32 s16, s50, 0xfc00000
	s_addc_u32 s17, s51, 0
	s_lshl_b32 s1, s33, 1
	v_writelane_b32 v252, s2, 12
	v_mov_b32_e32 v1, v0
	s_and_b32 s1, s1, 0xff0
	s_lshl_b32 s2, s33, 11
	s_sub_i32 s1, 0x870, s1
	v_lshrrev_b32_e32 v3, 3, v1
	s_and_b32 s2, s2, 0x3800
	v_bfe_u32 v2, v1, 2, 1
	v_and_b32_e32 v3, 2, v3
	s_add_i32 s3, s1, s2
	v_and_b32_e32 v4, 3, v1
	v_lshrrev_b32_e32 v5, 1, v1
	v_or3_b32 v178, v2, v3, s3
	v_mov_b32_e32 v179, 0
	v_and_or_b32 v4, v5, 4, v4
	v_lshlrev_b64 v[2:3], 13, v[178:179]
	v_bfe_u32 v10, v1, 5, 1
	v_lshl_add_u64 v[2:3], s[38:39], 0, v[2:3]
	v_lshlrev_b32_e32 v178, 7, v4
	v_lshlrev_b32_e32 v4, 4, v10
	v_mov_b32_e32 v5, v179
	v_lshl_add_u64 v[2:3], v[2:3], 0, v[178:179]
	v_lshl_add_u64 v[2:3], v[2:3], 0, v[4:5]
	s_mov_b64 s[4:5], 0x1600
	v_lshl_add_u64 v[6:7], v[2:3], 0, s[4:5]
	s_movk_i32 s4, 0x1000
	v_add_co_u32_e32 v8, vcc, s4, v2
	s_mov_b64 s[6:7], 0x9600
	s_nop 0
	v_addc_co_u32_e32 v9, vcc, 0, v3, vcc
	s_mov_b32 s5, 0x9000
	global_load_dwordx4 v[34:37], v[6:7], off offset:32
	global_load_dwordx4 v[38:41], v[6:7], off offset:64
	global_load_dwordx4 v[42:45], v[8:9], off offset:1536
	global_load_dwordx4 v[46:49], v[6:7], off offset:96
	v_lshl_add_u64 v[6:7], v[2:3], 0, s[6:7]
	v_add_co_u32_e32 v8, vcc, s5, v2
	s_mov_b64 s[6:7], 0x11600
	s_nop 0
	v_addc_co_u32_e32 v9, vcc, 0, v3, vcc
	global_load_dwordx4 v[50:53], v[6:7], off offset:32
	global_load_dwordx4 v[54:57], v[6:7], off offset:64
	global_load_dwordx4 v[58:61], v[8:9], off offset:1536
	global_load_dwordx4 v[62:65], v[6:7], off offset:96
	v_lshl_add_u64 v[6:7], v[2:3], 0, s[6:7]
	s_mov_b32 s6, 0x11000
	v_add_co_u32_e32 v8, vcc, s6, v2
	s_mov_b64 s[8:9], 0x19600
	s_nop 0
	v_addc_co_u32_e32 v9, vcc, 0, v3, vcc
	s_mov_b32 s7, 0x19000
	global_load_dwordx4 v[66:69], v[6:7], off offset:32
	global_load_dwordx4 v[70:73], v[6:7], off offset:64
	global_load_dwordx4 v[74:77], v[8:9], off offset:1536
	global_load_dwordx4 v[78:81], v[6:7], off offset:96
	v_lshl_add_u64 v[6:7], v[2:3], 0, s[8:9]
	v_add_co_u32_e32 v2, vcc, s7, v2
	v_or_b32_e32 v178, s3, v10
	s_nop 0
	v_addc_co_u32_e32 v3, vcc, 0, v3, vcc
	global_load_dwordx4 v[82:85], v[6:7], off offset:32
	global_load_dwordx4 v[86:89], v[6:7], off offset:64
	global_load_dwordx4 v[90:93], v[2:3], off offset:1536
	global_load_dwordx4 v[94:97], v[6:7], off offset:96
	v_lshlrev_b64 v[2:3], 13, v[178:179]
	v_lshl_add_u64 v[2:3], s[38:39], 0, v[2:3]
	v_add_co_u32_e32 v6, vcc, s4, v2
	s_movk_i32 s3, 0x5000
	s_nop 0
	v_addc_co_u32_e32 v7, vcc, 0, v3, vcc
	v_add_co_u32_e32 v8, vcc, s3, v2
	s_mov_b32 s3, 0xd000
	s_nop 0
	v_addc_co_u32_e32 v9, vcc, 0, v3, vcc
	global_load_dwordx4 v[98:101], v[6:7], off offset:3984
	global_load_dwordx4 v[102:105], v[8:9], off offset:3984
	v_add_co_u32_e32 v6, vcc, s5, v2
	v_readfirstlane_b32 s0, v1
	s_nop 0
	v_addc_co_u32_e32 v7, vcc, 0, v3, vcc
	v_add_co_u32_e32 v8, vcc, s3, v2
	s_mov_b32 s3, 0x15000
	s_nop 0
	v_addc_co_u32_e32 v9, vcc, 0, v3, vcc
	global_load_dwordx4 v[106:109], v[6:7], off offset:3984
	global_load_dwordx4 v[110:113], v[8:9], off offset:3984
	v_add_co_u32_e32 v6, vcc, s6, v2
	s_bfe_u32 s0, s0, 0x30006
	s_nop 0
	v_addc_co_u32_e32 v7, vcc, 0, v3, vcc
	v_add_co_u32_e32 v8, vcc, s3, v2
	s_mov_b32 s3, 0x1d000
	s_nop 0
	v_addc_co_u32_e32 v9, vcc, 0, v3, vcc
	global_load_dwordx4 v[114:117], v[6:7], off offset:3984
	global_load_dwordx4 v[118:121], v[8:9], off offset:3984
	v_add_co_u32_e32 v6, vcc, s7, v2
	s_lshr_b32 s1, s1, 5
	s_nop 0
	v_addc_co_u32_e32 v7, vcc, 0, v3, vcc
	v_add_co_u32_e32 v2, vcc, s3, v2
	s_lshl_b32 s3, s0, 5
	s_cmp_le_u32 s0, s1
	s_cselect_b32 s0, s3, 0
	v_and_or_b32 v1, v1, 31, s0
	v_or_b32_e32 v1, s2, v1
	v_addc_co_u32_e32 v3, vcc, 0, v3, vcc
	v_lshlrev_b32_e32 v178, 7, v1
	global_load_dwordx4 v[122:125], v[6:7], off offset:3984
	global_load_dwordx4 v[126:129], v[2:3], off offset:3984
	v_lshl_add_u64 v[2:3], s[16:17], 0, v[178:179]
	v_lshl_add_u64 v[2:3], v[2:3], 0, v[4:5]
	global_load_dwordx4 v[130:133], v[2:3], off
	global_load_dwordx4 v[134:137], v[2:3], off offset:32
	global_load_dwordx4 v[138:141], v[2:3], off offset:64
	global_load_dwordx4 v[142:145], v[2:3], off offset:96
	s_add_i32 s0, 0, 0x10000
	v_writelane_b32 v252, s0, 13
	v_writelane_b32 v252, s88, 14
	s_mov_b32 s40, 0
	s_add_i32 s97, 0, 0x26d80
	v_writelane_b32 v252, s89, 15
	v_writelane_b32 v252, s90, 16
	v_writelane_b32 v252, s91, 17
	v_writelane_b32 v252, s92, 18
	s_brev_b32 s30, 1
	v_mov_b32_e32 v1, 1
	v_writelane_b32 v252, s93, 19
	v_mov_b32_e32 v184, 0x7f61b1e6
	v_mov_b32_e32 v185, 0x10000
	v_writelane_b32 v252, s16, 20
	s_nop 1
	v_writelane_b32 v252, s17, 21
	s_waitcnt vmcnt(0)
	s_branch .LBB0_567

.LBB0_567:
	v_mov_b32_e32 v186, 0
	s_and_saveexec_b64 s[0:1], s[94:95]
	s_cbranch_execz .LBB0_571
	v_mov_b32_e32 v3, 1
	v_readlane_b32 s4, v252, 10
	v_readlane_b32 s5, v252, 11
	s_nop 4
	global_atomic_add v186, v179, v3, s[4:5] sc0

.LBB0_576:
	s_and_saveexec_b64 s[0:1], s[94:95]
	v_mov_b32_e32 v2, s97
	s_waitcnt vmcnt(0)
	v_add_u32_e32 v186, 64, v186
	ds_write_b32 v2, v186
	s_or_b64 exec, exec, s[0:1]
	s_waitcnt lgkmcnt(0)
	s_barrier
	v_mov_b32_e32 v2, s97
	ds_read_b32 v2, v2
	s_xor_b32 s97, s97, 4
	s_movk_i32 s0, 0x43f
	s_waitcnt lgkmcnt(0)
	v_cmp_lt_i32_e64 s[18:19], s0, v2
	v_readfirstlane_b32 s33, v2
	s_and_b64 vcc, exec, s[18:19]
	s_cbranch_vccnz .LBB0_580
	s_sub_i32 s0, s33, 64
	s_ashr_i32 s1, s0, 31
	s_lshr_b32 s1, s1, 29
	s_add_i32 s1, s0, s1
	s_and_b32 s2, s1, -8
	s_lshl_b32 s1, s1, 1
	s_sub_i32 s0, s0, s2
	v_mov_b32_e32 v12, v0
	s_and_b32 s1, s1, -16
	s_sub_i32 s3, 0x7f0, s1
	v_readfirstlane_b32 s2, v12
	s_ashr_i32 s1, s0, 31
	s_bfe_u32 s2, s2, 0x30006
	s_lshl_b64 s[0:1], s[0:1], 11
	v_lshrrev_b32_e32 v3, 3, v12
	s_add_u32 s5, s0, s3
	v_bfe_u32 v2, v12, 2, 1
	v_and_b32_e32 v3, 2, v3
	s_addc_u32 s6, s1, 0
	v_and_b32_e32 v4, 3, v12
	v_lshrrev_b32_e32 v5, 1, v12
	v_or3_b32 v2, v2, v3, s5
	v_mov_b32_e32 v3, s6
	v_and_or_b32 v6, v5, 4, v4
	v_lshlrev_b64 v[4:5], 13, v[2:3]
	v_bfe_u32 v13, v12, 5, 1
	v_lshl_add_u64 v[4:5], s[38:39], 0, v[4:5]
	v_lshlrev_b32_e32 v178, 7, v6
	v_lshlrev_b32_e32 v6, 4, v13
	v_mov_b32_e32 v7, v179
	v_lshl_add_u64 v[4:5], v[4:5], 0, v[178:179]
	v_lshl_add_u64 v[4:5], v[4:5], 0, v[6:7]
	s_mov_b64 s[6:7], 0x1600
	v_lshl_add_u64 v[8:9], v[4:5], 0, s[6:7]
	s_movk_i32 s6, 0x1000
	v_add_co_u32_e32 v10, vcc, s6, v4
	s_mov_b64 s[8:9], 0x9600
	s_nop 0
	v_addc_co_u32_e32 v11, vcc, 0, v5, vcc
	s_mov_b32 s7, 0x9000
	global_load_dwordx4 v[34:37], v[8:9], off offset:32
	global_load_dwordx4 v[38:41], v[8:9], off offset:64
	global_load_dwordx4 v[42:45], v[10:11], off offset:1536
	global_load_dwordx4 v[46:49], v[8:9], off offset:96
	v_lshl_add_u64 v[8:9], v[4:5], 0, s[8:9]
	v_add_co_u32_e32 v10, vcc, s7, v4
	s_mov_b64 s[8:9], 0x11600
	s_nop 0
	v_addc_co_u32_e32 v11, vcc, 0, v5, vcc
	global_load_dwordx4 v[50:53], v[8:9], off offset:32
	global_load_dwordx4 v[54:57], v[8:9], off offset:64
	global_load_dwordx4 v[58:61], v[10:11], off offset:1536
	global_load_dwordx4 v[62:65], v[8:9], off offset:96
	v_lshl_add_u64 v[8:9], v[4:5], 0, s[8:9]
	s_mov_b32 s8, 0x11000
	v_add_co_u32_e32 v10, vcc, s8, v4
	s_mov_b64 s[10:11], 0x19600
	s_nop 0
	v_addc_co_u32_e32 v11, vcc, 0, v5, vcc
	s_mov_b32 s9, 0x19000
	v_or_b32_e32 v2, s5, v13
	global_load_dwordx4 v[66:69], v[8:9], off offset:32
	global_load_dwordx4 v[70:73], v[8:9], off offset:64
	global_load_dwordx4 v[74:77], v[10:11], off offset:1536
	global_load_dwordx4 v[78:81], v[8:9], off offset:96
	v_lshl_add_u64 v[8:9], v[4:5], 0, s[10:11]
	v_add_co_u32_e32 v4, vcc, s9, v4
	v_lshlrev_b64 v[2:3], 13, v[2:3]
	s_nop 0
	v_addc_co_u32_e32 v5, vcc, 0, v5, vcc
	v_lshl_add_u64 v[2:3], s[38:39], 0, v[2:3]
	global_load_dwordx4 v[82:85], v[8:9], off offset:32
	global_load_dwordx4 v[86:89], v[8:9], off offset:64
	global_load_dwordx4 v[90:93], v[4:5], off offset:1536
	global_load_dwordx4 v[94:97], v[8:9], off offset:96
	v_add_co_u32_e32 v4, vcc, s6, v2
	s_movk_i32 s5, 0x5000
	s_nop 0
	v_addc_co_u32_e32 v5, vcc, 0, v3, vcc
	v_add_co_u32_e32 v8, vcc, s5, v2
	s_mov_b32 s5, 0xd000
	s_nop 0
	v_addc_co_u32_e32 v9, vcc, 0, v3, vcc
	global_load_dwordx4 v[98:101], v[4:5], off offset:3984
	global_load_dwordx4 v[102:105], v[8:9], off offset:3984
	v_add_co_u32_e32 v4, vcc, s7, v2
	s_lshr_b32 s3, s3, 5
	s_nop 0
	v_addc_co_u32_e32 v5, vcc, 0, v3, vcc
	v_add_co_u32_e32 v8, vcc, s5, v2
	s_mov_b32 s5, 0x15000
	s_nop 0
	v_addc_co_u32_e32 v9, vcc, 0, v3, vcc
	global_load_dwordx4 v[106:109], v[4:5], off offset:3984
	global_load_dwordx4 v[110:113], v[8:9], off offset:3984
	v_add_co_u32_e32 v4, vcc, s8, v2
	s_nop 1
	v_addc_co_u32_e32 v5, vcc, 0, v3, vcc
	v_add_co_u32_e32 v8, vcc, s5, v2
	s_mov_b32 s5, 0x1d000
	s_nop 0
	v_addc_co_u32_e32 v9, vcc, 0, v3, vcc
	global_load_dwordx4 v[114:117], v[4:5], off offset:3984
	global_load_dwordx4 v[118:121], v[8:9], off offset:3984
	v_add_co_u32_e32 v4, vcc, s9, v2
	s_nop 1
	v_addc_co_u32_e32 v5, vcc, 0, v3, vcc
	v_add_co_u32_e32 v2, vcc, s5, v2
	s_lshl_b32 s5, s2, 5
	s_cmp_le_u32 s2, s3
	s_cselect_b32 s2, s5, 0
	v_addc_co_u32_e32 v3, vcc, 0, v3, vcc
	global_load_dwordx4 v[122:125], v[4:5], off offset:3984
	global_load_dwordx4 v[126:129], v[2:3], off offset:3984
	v_and_or_b32 v2, v12, 31, s2
	v_or_b32_e32 v2, s0, v2
	v_mov_b32_e32 v3, s1
	v_lshlrev_b64 v[2:3], 7, v[2:3]
	v_lshl_add_u64 v[2:3], s[16:17], 0, v[2:3]
	v_lshl_add_u64 v[2:3], v[2:3], 0, v[6:7]
	global_load_dwordx4 v[130:133], v[2:3], off
	global_load_dwordx4 v[134:137], v[2:3], off offset:32
	global_load_dwordx4 v[138:141], v[2:3], off offset:64
	global_load_dwordx4 v[142:145], v[2:3], off offset:96

.LBB0_1238:
	s_waitcnt vmcnt(0)
	v_lshlrev_b32_e32 v178, 3, v146
	s_ashr_i32 s91, s90, 31
	v_lshl_add_u64 v[6:7], s[56:57], 0, v[178:179]
	s_mov_b32 s93, s40
	s_lshl_b64 s[2:3], s[90:91], 19
	s_lshl_b64 s[4:5], s[92:93], 8
	v_lshl_add_u64 v[6:7], v[6:7], 0, s[2:3]
	v_lshl_add_u64 v[6:7], v[6:7], 0, s[4:5]
	global_store_dwordx2 v[6:7], v[2:3], off
	global_store_dwordx2 v[6:7], v[4:5], off offset:256
	s_branch .LBB0_566

.LBB0_1294:
	s_getpc_b64 s[98:99]
	s_and_b32 s98, s98, 0xffffff80
	v_readlane_b32 s97, v252, 2
	s_nop 0
	s_and_b32 s97, s97, 31
	s_mul_i32 s97, s97, 0x300
	s_add_u32 s98, s98, s97
	s_addc_u32 s99, s99, 0
	v_and_b32_e32 v254, 63, v0
	v_min_u32_e32 v254, 5, v254
	v_lshlrev_b32_e32 v254, 7, v254
	global_load_dword v254, v254, s[98:99]
	s_cmp_lt_i32 s88, 5
	s_cselect_b64 s[0:1], -1, 0
	s_cmp_gt_i32 s89, 4
	s_cselect_b64 s[4:5], -1, 0
	s_and_b64 s[0:1], s[0:1], s[4:5]
	s_andn2_b64 vcc, exec, s[0:1]
	s_cbranch_vccnz .LBB0_1427
	s_mov_b32 s98, 0
	v_readlane_b32 s99, v252, 2
	s_nop 0
	s_bitcmp1_b32 s99, 0
	s_cbranch_scc0 .Lp2c_oa
	s_mov_b32 s98, 1
	v_readlane_b32 s68, v252, 2
	s_branch .LBB0_1314
.Lp2c_oa:
	s_cmp_lg_u32 s90, -1
	s_cselect_b64 s[0:1], -1, 0
	s_cmpk_lt_i32 s96, 0x4000
	s_cselect_b64 s[4:5], -1, 0
	s_and_b64 s[0:1], s[0:1], s[4:5]
	s_andn2_b64 vcc, exec, s[0:1]
	v_readlane_b32 s68, v252, 2
	s_cbranch_vccnz .LBB0_1314
	s_abs_i32 s3, s92
	v_cvt_f32_u32_e32 v1, s3
	s_sub_i32 s4, 0, s3
	v_readlane_b32 s1, v252, 6
	s_sub_i32 s1, s92, s1
	v_rcp_iflag_f32_e32 v1, v1
	s_ashr_i32 s93, s92, 31
	s_ashr_i32 s97, s96, 31
	s_lshl_b32 s0, s84, 5
	v_mul_f32_e32 v1, 0x4f7ffffe, v1
	v_cvt_u32_f32_e32 v1, v1
	s_lshl_b64 s[18:19], s[92:93], 12
	s_lshl_b64 s[20:21], s[96:97], 13
	s_mul_i32 s24, s92, 0x6000
	v_readfirstlane_b32 s5, v1
	s_mul_i32 s4, s4, s5
	s_mul_hi_u32 s4, s5, s4
	s_add_i32 s33, s5, s4
	v_readlane_b32 s4, v252, 7
	s_sub_i32 s1, s1, s4
	s_add_i32 s34, s1, 0x3fff
	s_add_u32 s1, s50, s20
	s_addc_u32 s5, s51, s21
	s_add_u32 s4, s1, 0x1800c00
	s_addc_u32 s5, s5, 0
	s_ashr_i32 s1, s0, 31
	s_lshl_b64 s[6:7], s[0:1], 13
	s_lshl_b64 s[22:23], s[96:97], 11
	s_add_u32 s8, s50, s22
	s_addc_u32 s9, s51, s23
	s_add_u32 s8, s8, 0xbc00000
	s_addc_u32 s9, s9, 0
	s_lshl_b64 s[10:11], s[0:1], 11
	s_add_u32 s14, s92, s96
	s_addc_u32 s15, s93, s97
	s_lshl_b64 s[12:13], s[14:15], 13
	s_add_u32 s1, s50, s12
	s_addc_u32 s13, s51, s13
	s_add_u32 s12, s1, 0x1800c00
	s_addc_u32 s13, s13, 0
	s_lshl_b64 s[14:15], s[14:15], 11
	s_add_u32 s1, s50, s14
	s_addc_u32 s15, s51, s15
	s_add_u32 s14, s1, 0xbc00000
	s_addc_u32 s15, s15, 0
	s_lshl_b64 s[16:17], s[92:93], 14
	s_add_u32 s1, s16, s20
	s_addc_u32 s16, s17, s21
	s_add_u32 s1, s50, s1
	s_addc_u32 s17, s51, s16
	s_add_u32 s16, s1, 0x1800c00
	s_addc_u32 s17, s17, 0
	s_add_u32 s1, s18, s22
	s_addc_u32 s18, s19, s23
	s_add_u32 s1, s50, s1
	s_addc_u32 s19, s51, s18
	s_add_u32 s18, s1, 0xbc00000
	s_addc_u32 s19, s19, 0
	s_mul_hi_i32 s1, s92, 0x6000
	s_add_u32 s20, s24, s20
	s_addc_u32 s1, s1, s21
	s_add_u32 s20, s50, s20
	s_addc_u32 s1, s51, s1
	s_add_u32 s20, s20, 0x1800c00
	s_addc_u32 s21, s1, 0
	s_mul_i32 s24, s92, 0x1800
	s_mul_hi_i32 s1, s92, 0x1800
	s_add_u32 s22, s24, s22
	s_addc_u32 s1, s1, s23
	s_add_u32 s22, s50, s22
	v_lshlrev_b32_e32 v2, 5, v198
	s_addc_u32 s1, s51, s1
	s_waitcnt vmcnt(0)
	v_mov_b32_e32 v43, 0
	v_and_b32_e32 v42, 0x1e0, v2
	s_add_u32 s22, s22, 0xbc00000
	v_mbcnt_lo_u32_b32 v2, -1, 0
	v_lshl_add_u64 v[44:45], s[64:65], 0, v[42:43]
	v_lshlrev_b32_e32 v42, 4, v198
	s_addc_u32 s23, s1, 0
	v_mov_b32_e32 v1, 0x358637bd
	v_mbcnt_hi_u32_b32 v48, -1, v2
	s_branch .LBB0_1298

.LBB0_1314:
	s_cmpk_gt_i32 s68, 0xff
	s_cbranch_scc1 .LBB0_1373
	v_mbcnt_lo_u32_b32 v1, -1, 0
	s_waitcnt vmcnt(0)
	v_mbcnt_hi_u32_b32 v92, -1, v1
	v_and_b32_e32 v1, 64, v92
	v_readlane_b32 s24, v252, 8
	v_mov_b32_e32 v87, 0
	s_mov_b64 s[0:1], 0x1a00
	s_movk_i32 s3, 0x1000
	s_mov_b64 s[4:5], 0x1c00
	s_movk_i32 s14, 0x800
	v_mov_b32_e32 v94, 0x9000
	s_movk_i32 s15, 0xf7ff
	s_mov_b32 s16, 0x3e38aa3b
	s_mov_b32 s17, 0x7f61b1e6
	v_xor_b32_e32 v95, 32, v92
	v_add_u32_e32 v93, 64, v1
	s_mov_b32 s18, s68
	v_readlane_b32 s25, v252, 9
	s_cmp_eq_u32 s98, 2
	s_cbranch_scc1 .Lp2c_dsa2

.Lp2c_memdone:
	s_cmp_eq_u32 s98, 1
	s_cbranch_scc0 .Lp2c_dsa
	s_mov_b32 s98, 2
	v_mov_b32_e32 v251, v1
	s_branch .Lp2c_oa
.Lp2c_dsa2:
	v_mov_b32_e32 v1, v251
.Lp2c_dsa:
	v_xor_b32_e32 v2, 1, v92
	v_cmp_lt_i32_e32 vcc, v2, v93
	s_add_u32 s6, s50, 0x1400000
	s_addc_u32 s7, s51, 0
	v_cndmask_b32_e32 v2, v92, v2, vcc
	v_lshlrev_b32_e32 v136, 2, v2
	v_xor_b32_e32 v2, 2, v92
	v_cmp_lt_i32_e32 vcc, v2, v93
	s_add_u32 s8, s50, 0xd80000
	s_addc_u32 s9, s51, 0
	v_cndmask_b32_e32 v2, v92, v2, vcc
	v_lshlrev_b32_e32 v137, 2, v2
	v_xor_b32_e32 v2, 4, v92
	v_cmp_lt_i32_e32 vcc, v2, v93
	s_movk_i32 s3, 0x800
	s_movk_i32 s30, 0x200
	v_cndmask_b32_e32 v2, v92, v2, vcc
	v_lshlrev_b32_e32 v138, 2, v2
	v_xor_b32_e32 v2, 8, v92
	v_cmp_lt_i32_e32 vcc, v2, v93
	s_movk_i32 s31, 0x600
	s_movk_i32 s33, 0x400
	v_cndmask_b32_e32 v2, v92, v2, vcc
	v_lshlrev_b32_e32 v139, 2, v2
	v_xor_b32_e32 v2, 16, v92
	v_cmp_lt_i32_e32 vcc, v2, v93
	v_mov_b32_e32 v133, 0
	s_mov_b64 s[10:11], 0x1000
	v_cndmask_b32_e32 v2, v92, v2, vcc
	v_lshlrev_b32_e32 v140, 2, v2
	s_movk_i32 s34, 0x1000
	s_mov_b32 s13, 0
	s_movk_i32 s35, 0x100
	s_movk_i32 s36, 0x2000
	s_movk_i32 s37, 0x104
	s_mov_b32 s40, 0xf800000
	v_mov_b32_e32 v141, 0x260
	s_mov_b32 s41, 0x7f61b1e6
	s_mov_b64 s[14:15], 0x1400
	s_movk_i32 s42, 0x3000
	s_movk_i32 s43, 0x410
	v_mov_b32_e32 v142, 0xc6ea
	v_mov_b32_e32 v143, 0xc6ea0000
	v_mov_b32_e32 v144, 0x3f80
	s_branch .LBB0_1321

.LBB0_1341:
	s_or_b64 exec, exec, s[22:23]
	v_lshlrev_b32_e32 v2, 2, v14
	v_and_b32_e32 v2, 12, v2
	v_bfe_u32 v3, v14, 2, 2
	v_bitop3_b32 v2, v2, v23, v3 bitop3:0x36
	v_lshlrev_b32_e32 v67, 8, v14
	v_lshlrev_b32_e32 v3, 4, v2
	v_or_b32_e32 v2, v3, v67
	s_ashr_i32 s23, s61, 8
	v_add_u32_e32 v2, 0, v2
	s_waitcnt vmcnt(0)
	ds_write_b128 v2, v[116:119]
	ds_write_b128 v2, v[120:123] offset:8192
	s_lshl_b32 s4, s23, 13
	v_lshlrev_b32_e32 v2, 2, v145
	s_add_i32 s4, s4, 0
	v_and_b32_e32 v2, 12, v2
	v_bfe_u32 v7, v149, 2, 2
	v_lshl_add_u32 v8, v145, 8, s4
	v_bitop3_b32 v9, v2, v146, v7 bitop3:0x36
	v_lshl_add_u32 v150, v9, 4, v8
	v_or_b32_e32 v9, 2, v146
	v_bitop3_b32 v9, v2, v9, v7 bitop3:0x36
	v_lshl_add_u32 v151, v9, 4, v8
	v_or_b32_e32 v9, 4, v146
	v_bitop3_b32 v9, v2, v9, v7 bitop3:0x36
	v_lshl_add_u32 v152, v9, 4, v8
	v_or_b32_e32 v9, 6, v146
	v_bitop3_b32 v9, v2, v9, v7 bitop3:0x36
	v_lshl_add_u32 v153, v9, 4, v8
	v_or_b32_e32 v9, 8, v146
	v_bitop3_b32 v9, v2, v9, v7 bitop3:0x36
	v_lshl_add_u32 v154, v9, 4, v8
	v_or_b32_e32 v9, 10, v146
	v_bitop3_b32 v9, v2, v9, v7 bitop3:0x36
	v_lshl_add_u32 v155, v9, 4, v8
	v_or_b32_e32 v9, 12, v146
	v_bitop3_b32 v9, v2, v9, v7 bitop3:0x36
	v_lshl_add_u32 v156, v9, 4, v8
	v_or_b32_e32 v9, 14, v146
	v_bitop3_b32 v2, v2, v9, v7 bitop3:0x36
	v_lshl_add_u32 v158, v2, 4, v8
	v_lshrrev_b32_e32 v2, 3, v149
	v_bfe_u32 v8, v149, 1, 1
	v_lshlrev_b32_e32 v6, 2, v146
	v_and_or_b32 v2, v2, 2, v8
	v_lshlrev_b32_e32 v8, 2, v7
	v_lshlrev_b32_e32 v9, 3, v147
	v_or_b32_e32 v10, v6, v7
	v_bitop3_b32 v11, v8, v2, v146 bitop3:0x36
	v_and_b32_e32 v9, 8, v9
	v_lshlrev_b32_e32 v10, 8, v10
	v_lshl_add_u32 v11, v11, 4, s4
	v_or_b32_e32 v148, 8, v6
	v_add3_u32 v159, v11, v10, v9
	v_lshrrev_b32_e32 v11, 2, v148
	v_or_b32_e32 v7, v148, v7
	v_bitop3_b32 v12, v11, v2, v8 bitop3:0x36
	v_lshlrev_b32_e32 v7, 8, v7
	v_lshl_add_u32 v12, v12, 4, s4
	v_add3_u32 v160, v12, v7, v9
	v_or_b32_e32 v12, 4, v2
	v_bitop3_b32 v13, v8, v12, v146 bitop3:0x36
	v_bitop3_b32 v12, v11, v12, v8 bitop3:0x36
	v_lshl_add_u32 v12, v12, 4, s4
	v_lshl_add_u32 v13, v13, 4, s4
	v_add3_u32 v162, v12, v7, v9
	v_or_b32_e32 v12, 8, v2
	v_add3_u32 v161, v13, v10, v9
	v_bitop3_b32 v13, v8, v12, v146 bitop3:0x36
	v_bitop3_b32 v12, v11, v12, v8 bitop3:0x36
	v_lshl_add_u32 v12, v12, 4, s4
	v_or_b32_e32 v2, 12, v2
	v_add3_u32 v164, v12, v7, v9
	v_bitop3_b32 v12, v8, v2, v146 bitop3:0x36
	v_bitop3_b32 v2, v11, v2, v8 bitop3:0x36
	s_ashr_i32 s22, s12, 1
	v_lshl_add_u32 v13, v13, 4, s4
	v_lshl_add_u32 v12, v12, 4, s4
	v_lshl_add_u32 v2, v2, 4, s4
	v_add3_u32 v163, v13, v10, v9
	v_add3_u32 v165, v12, v10, v9
	v_add3_u32 v166, v2, v7, v9
	s_cmp_lt_i32 s22, 1
	s_mov_b32 s24, 0
	s_waitcnt lgkmcnt(0)
	s_barrier
	s_cbranch_scc1 .LBB0_1366
	s_add_i32 s4, s60, 1
	v_cvt_f32_i32_e32 v7, s4
	v_lshlrev_b32_e32 v167, 3, v146
	v_cmp_eq_u32_e32 vcc, v145, v167
	v_or_b32_e32 v9, 1, v167
	v_mul_f32_e32 v7, -2.0, v7
	v_exp_f32_e32 v7, v7
	v_cndmask_b32_e32 v8, 0, v144, vcc
	v_cmp_eq_u32_e32 vcc, v145, v9
	v_or_b32_e32 v169, 16, v167
	v_mul_f32_e32 v168, 0x3fb8aa3b, v7
	v_cndmask_b32_e64 v7, 0, 1.0, vcc
	v_or_b32_e32 v124, v7, v8
	v_or_b32_e32 v7, 2, v167
	v_cmp_eq_u32_e32 vcc, v145, v7
	v_or_b32_e32 v8, 3, v167
	v_sub_u32_e32 v6, v4, v6
	v_cndmask_b32_e32 v7, 0, v144, vcc
	v_cmp_eq_u32_e32 vcc, v145, v8
	v_cvt_f32_i32_e32 v185, v6
	v_add_f32_e32 v6, v21, v22
	v_cndmask_b32_e64 v8, 0, 1.0, vcc
	v_or_b32_e32 v125, v8, v7
	v_or_b32_e32 v7, 4, v167
	v_cmp_eq_u32_e32 vcc, v145, v7
	v_or_b32_e32 v8, 5, v167
	v_max_f32_e32 v5, v5, v5
	v_cndmask_b32_e32 v7, 0, v144, vcc
	v_cmp_eq_u32_e32 vcc, v145, v8
	s_lshl_b32 s26, s23, 2
	s_add_i32 s26, s26, 0
	v_cndmask_b32_e64 v8, 0, 1.0, vcc
	v_or_b32_e32 v126, v8, v7
	v_or_b32_e32 v7, 6, v167
	v_cmp_eq_u32_e32 vcc, v145, v7
	v_or_b32_e32 v8, 7, v167
	v_add_u32_e32 v189, 0, v3
	v_cndmask_b32_e32 v7, 0, v144, vcc
	v_cmp_eq_u32_e32 vcc, v145, v8
	v_mov_b32_e32 v2, 0
	v_mov_b32_e32 v16, v2
	v_cndmask_b32_e64 v8, 0, 1.0, vcc
	v_or_b32_e32 v127, v8, v7
	v_cmp_eq_u32_e32 vcc, v145, v169
	v_or_b32_e32 v8, 17, v167
	v_mov_b32_e32 v17, v2
	v_cndmask_b32_e32 v7, 0, v144, vcc
	v_cmp_eq_u32_e32 vcc, v145, v8
	v_subrev_u32_e32 v187, 31, v4
	v_mov_b32_e32 v4, v2
	v_cndmask_b32_e64 v8, 0, 1.0, vcc
	v_or_b32_e32 v128, v8, v7
	v_or_b32_e32 v7, 18, v167
	v_cmp_eq_u32_e32 vcc, v145, v7
	v_or_b32_e32 v8, 19, v167
	v_mov_b32_e32 v10, v2
	v_cndmask_b32_e32 v7, 0, v144, vcc
	v_cmp_eq_u32_e32 vcc, v145, v8
	v_mov_b32_e32 v11, v2
	v_mov_b32_e32 v12, v2
	v_cndmask_b32_e64 v8, 0, 1.0, vcc
	v_or_b32_e32 v129, v8, v7
	v_or_b32_e32 v7, 20, v167
	v_cmp_eq_u32_e32 vcc, v145, v7
	v_or_b32_e32 v8, 21, v167
	v_mov_b32_e32 v13, v2
	v_cndmask_b32_e32 v7, 0, v144, vcc
	v_cmp_eq_u32_e32 vcc, v145, v8
	v_mov_b32_e32 v14, v2
	v_mov_b32_e32 v15, v2
	v_cndmask_b32_e64 v8, 0, 1.0, vcc
	v_or_b32_e32 v130, v8, v7
	v_or_b32_e32 v7, 22, v167
	v_cmp_eq_u32_e32 vcc, v145, v7
	v_or_b32_e32 v8, 23, v167
	v_mul_f32_e32 v170, 0, v168
	v_cndmask_b32_e32 v7, 0, v144, vcc
	v_cmp_eq_u32_e32 vcc, v145, v8
	v_add_f32_e32 v171, v168, v168
	v_mul_f32_e32 v172, 0x40400000, v168
	v_cndmask_b32_e64 v8, 0, 1.0, vcc
	v_or_b32_e32 v131, v8, v7
	v_mul_f32_e32 v7, 0x4f800000, v6
	v_cmp_gt_f32_e32 vcc, s40, v6
	v_max_f32_e32 v8, v20, v20
	v_max_f32_e32 v5, v5, v8
	v_cndmask_b32_e32 v6, v6, v7, vcc
	v_sqrt_f32_e32 v7, v6
	v_mul_f32_e32 v173, 0x41000000, v168
	v_mul_f32_e32 v174, 0x41100000, v168
	v_mul_f32_e32 v175, 0x41200000, v168
	v_add_u32_e32 v8, -1, v7
	v_fma_f32 v9, -v8, v7, v6
	v_cmp_ge_f32_e64 s[4:5], 0, v9
	v_add_u32_e32 v9, 1, v7
	v_mul_f32_e32 v176, 0x41300000, v168
	v_cndmask_b32_e64 v8, v7, v8, s[4:5]
	v_fma_f32 v7, -v9, v7, v6
	v_cmp_lt_f32_e64 s[4:5], 0, v7
	v_mul_f32_e32 v177, 0x41800000, v168
	v_mul_f32_e32 v178, 0x41880000, v168
	v_cndmask_b32_e64 v7, v8, v9, s[4:5]
	s_lshl_b32 s5, s22, 3
	v_mul_f32_e32 v8, 0x37800000, v7
	s_add_i32 s5, s26, s5
	v_cndmask_b32_e32 v7, v7, v8, vcc
	v_cmp_class_f32_e32 vcc, v6, v141
	s_addk_i32 s5, 0x7ff8
	v_mov_b32_e32 v3, s5
	v_cndmask_b32_e32 v6, v7, v6, vcc
	v_mul_f32_e32 v6, 0x413504f3, v6
	v_mad_u32_u24 v190, v145, s37, v3
	s_lshl_b32 s26, s23, 5
	v_add3_u32 v3, s63, 33, v145
	v_mul_f32_e32 v5, v5, v6
	s_lshl_b32 s4, s22, 6
	v_subrev_u32_e32 v3, s26, v3
	v_mul_f32_e32 v5, 0x3e38aa3b, v5
	s_add_i32 s12, s4, 0xffffff80
	v_subrev_u32_e32 v191, s4, v3
	s_lshl_b32 s4, s22, 1
	v_mul_f32_e32 v186, 0x3f828f5c, v5
	s_add_i32 s4, s23, s4
	v_mov_b32_e32 v3, v2
	v_mov_b32_e32 v5, v2
	v_mov_b32_e32 v6, v2
	v_mov_b32_e32 v7, v2
	v_mov_b32_e32 v8, v2
	v_mov_b32_e32 v9, v2
	v_mov_b64_e32 v[64:65], v[16:17]
	v_mov_b64_e32 v[48:49], v[16:17]
	v_mov_b64_e32 v[32:33], v[16:17]
	v_mul_f32_e32 v179, 0x41900000, v168
	v_mul_f32_e32 v180, 0x41980000, v168
	v_mul_f32_e32 v181, 0x41c00000, v168
	v_mul_f32_e32 v182, 0x41c80000, v168
	v_mul_f32_e32 v183, 0x41d00000, v168
	v_mul_f32_e32 v184, 0x41d80000, v168
	v_mad_u32_u24 v188, v145, s37, 0
	s_add_i32 s25, s22, -1
	s_add_i32 s27, s4, -2
	v_mov_b32_e32 v157, 0xf149f2ca
	v_mov_b64_e32 v[62:63], v[14:15]
	v_mov_b64_e32 v[60:61], v[12:13]
	v_mov_b64_e32 v[58:59], v[10:11]
	v_mov_b64_e32 v[56:57], v[8:9]
	v_mov_b64_e32 v[54:55], v[6:7]
	v_mov_b64_e32 v[52:53], v[4:5]
	v_mov_b64_e32 v[50:51], v[2:3]
	v_mov_b64_e32 v[46:47], v[14:15]
	v_mov_b64_e32 v[44:45], v[12:13]
	v_mov_b64_e32 v[42:43], v[10:11]
	v_mov_b64_e32 v[40:41], v[8:9]
	v_mov_b64_e32 v[38:39], v[6:7]
	v_mov_b64_e32 v[36:37], v[4:5]
	v_mov_b64_e32 v[34:35], v[2:3]
	v_mov_b64_e32 v[30:31], v[14:15]
	v_mov_b64_e32 v[28:29], v[12:13]
	v_mov_b64_e32 v[26:27], v[10:11]
	v_mov_b64_e32 v[24:25], v[8:9]
	v_mov_b64_e32 v[22:23], v[6:7]
	v_mov_b64_e32 v[20:21], v[4:5]
	v_mov_b64_e32 v[18:19], v[2:3]
	v_mov_b32_e32 v66, v2
	s_cmp_lt_i32 s25, 1
	s_cbranch_scc1 .Ldsa_pro_nl
	v_lshl_add_u64 v[68:69], v[134:135], 0, s[12:13]
	v_lshlrev_b64 v[68:69], 8, v[68:69]
	v_lshl_add_u64 v[68:69], s[6:7], 0, v[68:69]
	v_lshl_add_u64 v[68:69], v[68:69], 0, v[132:133]
	v_add_co_u32_e32 v70, vcc, 0x2000, v68
	s_nop 1
	v_addc_co_u32_e32 v71, vcc, 0, v69, vcc
	global_load_dwordx4 v[116:119], v[68:69], off
	global_load_dwordx4 v[120:123], v[70:71], off
.Ldsa_pro_nl:
	s_branch .LBB0_1345
.LBB0_1343:
	s_waitcnt lgkmcnt(0)
	s_barrier

.LBB0_1345:
	s_cmp_lt_i32 s25, 1
	s_cbranch_scc1 .LBB0_1347
	v_add_u32_e32 v68, v189, v67
	s_waitcnt vmcnt(0)
	ds_write_b128 v68, v[116:119] offset:16384
	ds_write_b128 v68, v[120:123] offset:24576
	s_cmp_lt_i32 s25, 2
	s_cbranch_scc1 .LBB0_1347
	s_sub_i32 s70, s12, 64
	s_mov_b32 s71, s13
	v_lshl_add_u64 v[68:69], v[134:135], 0, s[70:71]
	v_lshlrev_b64 v[68:69], 8, v[68:69]
	v_lshl_add_u64 v[68:69], s[6:7], 0, v[68:69]
	v_lshl_add_u64 v[68:69], v[68:69], 0, v[132:133]
	v_add_co_u32_e32 v70, vcc, 0x2000, v68
	s_nop 1
	v_addc_co_u32_e32 v71, vcc, 0, v69, vcc
	global_load_dwordx4 v[116:119], v[68:69], off
	global_load_dwordx4 v[120:123], v[70:71], off

.LBB0_1352:
.LBB0_1354:
	s_add_i32 s4, s24, 1
	s_cmp_ge_i32 s4, s22
	s_waitcnt lgkmcnt(0)
	s_barrier
	s_cbranch_scc1 .LBB0_1344
	s_xor_b32 s28, s24, -2
	s_add_i32 s28, s28, s22
	s_cmp_lt_i32 s28, 1
	s_cbranch_scc1 .LBB0_1357
	v_add_u32_e32 v68, v189, v67
	s_waitcnt vmcnt(0)
	ds_write_b128 v68, v[116:119]
	ds_write_b128 v68, v[120:123] offset:8192
	s_cmp_lt_i32 s28, 2
	s_cbranch_scc1 .LBB0_1357
	s_lshl_b32 s29, s28, 6
	s_sub_i32 s64, s29, 0x80
	s_mov_b32 s65, s13
	v_lshl_add_u64 v[68:69], v[134:135], 0, s[64:65]
	v_lshlrev_b64 v[68:69], 8, v[68:69]
	v_lshl_add_u64 v[68:69], s[6:7], 0, v[68:69]
	v_lshl_add_u64 v[68:69], v[68:69], 0, v[132:133]
	v_add_co_u32_e32 v70, vcc, 0x2000, v68
	s_nop 1
	v_addc_co_u32_e32 v71, vcc, 0, v69, vcc
	global_load_dwordx4 v[116:119], v[68:69], off
	global_load_dwordx4 v[120:123], v[70:71], off

.LBB0_1361:
	ds_read_b64_tr_b16 v[76:77], v159 offset:16384
	ds_read_b64_tr_b16 v[80:81], v159 offset:20480
	ds_read_b64_tr_b16 v[78:79], v160 offset:16384
	ds_read_b64_tr_b16 v[82:83], v160 offset:20480
	ds_read_b64_tr_b16 v[202:203], v161 offset:16384
	ds_read_b64_tr_b16 v[206:207], v161 offset:20480
	ds_read_b64_tr_b16 v[204:205], v162 offset:16384
	ds_read_b64_tr_b16 v[208:209], v162 offset:20480
	ds_read_b64_tr_b16 v[210:211], v163 offset:16384
	ds_read_b64_tr_b16 v[214:215], v163 offset:20480
	ds_read_b64_tr_b16 v[212:213], v164 offset:16384
	ds_read_b64_tr_b16 v[216:217], v164 offset:20480
	ds_read_b64_tr_b16 v[218:219], v165 offset:16384
	ds_read_b64_tr_b16 v[222:223], v165 offset:20480
	ds_read_b64_tr_b16 v[220:221], v166 offset:16384
	ds_read_b64_tr_b16 v[224:225], v166 offset:20480
	v_mul_f32_e64 v201, v201, -v168
	v_sub_f32_e32 v201, v157, v201
	v_sub_f32_e32 v200, v200, v201
	v_exp_f32_e32 v200, v200
	v_sub_f32_e32 v199, v199, v201
	v_exp_f32_e32 v199, v199
	v_sub_f32_e32 v197, v197, v201
	v_exp_f32_e32 v197, v197
	v_sub_f32_e32 v196, v196, v201
	v_exp_f32_e32 v196, v196
	v_sub_f32_e32 v195, v195, v201
	v_add_f32_e32 v226, 0, v200
	v_exp_f32_e32 v195, v195
	v_sub_f32_e32 v194, v194, v201
	v_add_f32_e32 v226, v199, v226
	v_exp_f32_e32 v194, v194
	v_sub_f32_e32 v193, v193, v201
	v_add_f32_e32 v226, v197, v226
	v_exp_f32_e32 v193, v193
	v_sub_f32_e32 v192, v192, v201
	v_add_f32_e32 v226, v196, v226
	v_exp_f32_e32 v192, v192
	v_sub_f32_e32 v75, v75, v201
	v_add_f32_e32 v226, v195, v226
	v_exp_f32_e32 v75, v75
	v_sub_f32_e32 v74, v74, v201
	v_add_f32_e32 v226, v194, v226
	v_exp_f32_e32 v74, v74
	v_sub_f32_e32 v73, v73, v201
	v_add_f32_e32 v226, v193, v226
	v_exp_f32_e32 v73, v73
	v_sub_f32_e32 v72, v72, v201
	v_add_f32_e32 v226, v192, v226
	v_exp_f32_e32 v227, v72
	v_sub_f32_e32 v71, v71, v201
	v_add_f32_e32 v72, v75, v226
	v_exp_f32_e32 v226, v71
	v_sub_f32_e32 v70, v70, v201
	v_add_f32_e32 v72, v74, v72
	v_exp_f32_e32 v228, v70
	v_sub_f32_e32 v69, v69, v201
	v_add_f32_e32 v72, v73, v72
	v_exp_f32_e32 v229, v69
	v_sub_f32_e32 v68, v68, v201
	v_add_f32_e32 v72, v227, v72
	v_exp_f32_e32 v201, v68
	v_add_f32_e32 v68, v226, v72
	v_add_f32_e32 v68, v228, v68
	v_add_f32_e32 v68, v229, v68
	v_add_f32_e32 v68, v201, v68
	v_add_f32_e32 v66, v66, v68
	v_cvt_pk_bf16_f32 v68, v200, v199
	v_cvt_pk_bf16_f32 v69, v197, v196
	v_cvt_pk_bf16_f32 v70, v195, v194
	v_cvt_pk_bf16_f32 v71, v193, v192
	v_cvt_pk_bf16_f32 v72, v75, v74
	v_cvt_pk_bf16_f32 v73, v73, v227
	v_cvt_pk_bf16_f32 v74, v226, v228
	v_cvt_pk_bf16_f32 v75, v229, v201
	s_waitcnt lgkmcnt(13)
	v_mfma_f32_32x32x16_bf16 v[2:17], v[76:79], v[68:71], v[2:17]
	s_waitcnt lgkmcnt(9)
	v_mfma_f32_32x32x16_bf16 v[50:65], v[202:205], v[68:71], v[50:65]
	s_waitcnt lgkmcnt(5)
	v_mfma_f32_32x32x16_bf16 v[34:49], v[210:213], v[68:71], v[34:49]
	s_waitcnt lgkmcnt(1)
	v_mfma_f32_32x32x16_bf16 v[18:33], v[218:221], v[68:71], v[18:33]
	v_mfma_f32_32x32x16_bf16 v[2:17], v[80:83], v[72:75], v[2:17]
	v_mfma_f32_32x32x16_bf16 v[50:65], v[206:209], v[72:75], v[50:65]
	v_mfma_f32_32x32x16_bf16 v[34:49], v[214:217], v[72:75], v[34:49]
	s_waitcnt lgkmcnt(0)
	v_mfma_f32_32x32x16_bf16 v[18:33], v[222:225], v[72:75], v[18:33]
.LBB0_1362:
	s_branch .LBB0_1343
.LBB0_1364:
	s_or_b64 exec, exec, s[22:23]
	s_and_saveexec_b64 s[22:23], s[26:27]
	s_cbranch_execz .LBB0_1339
